# tconv8 epilogue: counted lgkmcnt waits at each store's first consumer instead of one lgkmcnt(0) before both stores; dead padding keeps later loops aligned
# baseline (speedup 1.0000x reference)
.Lt8z_0_0:
	s_waitcnt lgkmcnt(1)
	global_store_dwordx4 v[194:195], v[168:171], off
	s_waitcnt lgkmcnt(0)
	global_store_dwordx4 v[196:197], v[172:175], off
	s_nop 1
	v_lshlrev_b32_e32 v168, 16, v26
	v_and_b32_e32 v169, 0xffff0000, v26
	v_lshlrev_b32_e32 v170, 16, v27
	v_and_b32_e32 v171, 0xffff0000, v27
	v_lshlrev_b32_e32 v172, 16, v28
	v_and_b32_e32 v173, 0xffff0000, v28
	v_lshlrev_b32_e32 v174, 16, v29
	v_and_b32_e32 v175, 0xffff0000, v29
	v_pk_mul_f32 v[168:169], v[4:5], v[168:169] op_sel_hi:[0,1]
	v_pk_mul_f32 v[170:171], v[4:5], v[170:171] op_sel_hi:[0,1]
	v_pk_fma_f32 v[148:149], v[184:185], v[148:149], v[168:169] op_sel_hi:[0,1,1]
	v_pk_fma_f32 v[150:151], v[184:185], v[150:151], v[170:171] op_sel_hi:[0,1,1]
	v_pk_mul_f32 v[148:149], v[148:149], v[172:173]
	v_pk_mul_f32 v[150:151], v[150:151], v[174:175]
	v_cvt_pk_bf16_f32 v240, v148, v149
	v_cvt_pk_bf16_f32 v241, v150, v151
	ds_write_b64 v0, v[240:241]
	v_lshlrev_b32_e32 v168, 16, v30
	v_and_b32_e32 v169, 0xffff0000, v30
	v_lshlrev_b32_e32 v170, 16, v31
	v_and_b32_e32 v171, 0xffff0000, v31
	v_lshlrev_b32_e32 v172, 16, v32
	v_and_b32_e32 v173, 0xffff0000, v32
	v_lshlrev_b32_e32 v174, 16, v33
	v_and_b32_e32 v175, 0xffff0000, v33
	v_pk_mul_f32 v[168:169], v[4:5], v[168:169] op_sel_hi:[0,1]
	v_pk_mul_f32 v[170:171], v[4:5], v[170:171] op_sel_hi:[0,1]
	v_pk_fma_f32 v[144:145], v[184:185], v[144:145], v[168:169] op_sel_hi:[0,1,1]
	v_pk_fma_f32 v[146:147], v[184:185], v[146:147], v[170:171] op_sel_hi:[0,1,1]
	v_pk_mul_f32 v[144:145], v[144:145], v[172:173]
	v_pk_mul_f32 v[146:147], v[146:147], v[174:175]
	v_cvt_pk_bf16_f32 v240, v144, v145
	v_cvt_pk_bf16_f32 v241, v146, v147
	ds_write_b64 v0, v[240:241] offset:32
	v_lshlrev_b32_e32 v168, 16, v34
	v_and_b32_e32 v169, 0xffff0000, v34
	v_lshlrev_b32_e32 v170, 16, v35
	v_and_b32_e32 v171, 0xffff0000, v35
	v_lshlrev_b32_e32 v172, 16, v36
	v_and_b32_e32 v173, 0xffff0000, v36
	v_lshlrev_b32_e32 v174, 16, v37
	v_and_b32_e32 v175, 0xffff0000, v37
	v_pk_mul_f32 v[168:169], v[4:5], v[168:169] op_sel_hi:[0,1]
	v_pk_mul_f32 v[170:171], v[4:5], v[170:171] op_sel_hi:[0,1]
	v_pk_fma_f32 v[140:141], v[184:185], v[140:141], v[168:169] op_sel_hi:[0,1,1]
	v_pk_fma_f32 v[142:143], v[184:185], v[142:143], v[170:171] op_sel_hi:[0,1,1]
	v_pk_mul_f32 v[140:141], v[140:141], v[172:173]
	v_pk_mul_f32 v[142:143], v[142:143], v[174:175]
	v_cvt_pk_bf16_f32 v240, v140, v141
	v_cvt_pk_bf16_f32 v241, v142, v143
	ds_write_b64 v0, v[240:241] offset:64
	v_lshlrev_b32_e32 v168, 16, v236
	v_and_b32_e32 v169, 0xffff0000, v236
	v_lshlrev_b32_e32 v170, 16, v237
	v_and_b32_e32 v171, 0xffff0000, v237
	v_lshlrev_b32_e32 v172, 16, v238
	v_and_b32_e32 v173, 0xffff0000, v238
	v_lshlrev_b32_e32 v174, 16, v239
	v_and_b32_e32 v175, 0xffff0000, v239
	v_pk_mul_f32 v[168:169], v[4:5], v[168:169] op_sel_hi:[0,1]
	v_pk_mul_f32 v[170:171], v[4:5], v[170:171] op_sel_hi:[0,1]
	v_pk_fma_f32 v[136:137], v[184:185], v[136:137], v[168:169] op_sel_hi:[0,1,1]
	v_pk_fma_f32 v[138:139], v[184:185], v[138:139], v[170:171] op_sel_hi:[0,1,1]
	v_pk_mul_f32 v[136:137], v[136:137], v[172:173]
	v_pk_mul_f32 v[138:139], v[138:139], v[174:175]
	v_cvt_pk_bf16_f32 v240, v136, v137
	v_cvt_pk_bf16_f32 v241, v138, v139
	ds_write_b64 v0, v[240:241] offset:96
	ds_read_b128 v[168:171], v1
	ds_read_b128 v[172:175], v1 offset:1152
	s_cbranch_vccz .Lt8z_0_1
	v_med3_f32 v248, v148, s77, v252
	v_med3_f32 v249, v149, s77, v252
	v_med3_f32 v250, v150, s77, v252
	v_med3_f32 v251, v151, s77, v252
	v_mov_b32_e32 v246, v245
	v_cvt_pk_fp8_f32 v246, v248, v249
	v_cvt_pk_fp8_f32 v246, v250, v251 op_sel:[0,0,1]
	ds_write_b32 v38, v246 offset:64
	v_med3_f32 v248, v144, s77, v252
	v_med3_f32 v249, v145, s77, v252
	v_med3_f32 v250, v146, s77, v252
	v_med3_f32 v251, v147, s77, v252
	v_mov_b32_e32 v246, v245
	v_cvt_pk_fp8_f32 v246, v248, v249
	v_cvt_pk_fp8_f32 v246, v250, v251 op_sel:[0,0,1]
	ds_write_b32 v38, v246 offset:80
	v_med3_f32 v248, v140, s77, v252
	v_med3_f32 v249, v141, s77, v252
	v_med3_f32 v250, v142, s77, v252
	v_med3_f32 v251, v143, s77, v252
	v_mov_b32_e32 v246, v245
	v_cvt_pk_fp8_f32 v246, v248, v249
	v_cvt_pk_fp8_f32 v246, v250, v251 op_sel:[0,0,1]
	ds_write_b32 v38, v246 offset:96
	v_med3_f32 v248, v136, s77, v252
	v_med3_f32 v249, v137, s77, v252
	v_med3_f32 v250, v138, s77, v252
	v_med3_f32 v251, v139, s77, v252
	v_mov_b32_e32 v246, v245
	v_cvt_pk_fp8_f32 v246, v248, v249
	v_cvt_pk_fp8_f32 v246, v250, v251 op_sel:[0,0,1]
	ds_write_b32 v38, v246 offset:112
.Lt8z_0_1:
	s_waitcnt lgkmcnt(1)
	global_store_dwordx4 v[194:195], v[168:171], off offset:128
	s_waitcnt lgkmcnt(0)
	global_store_dwordx4 v[196:197], v[172:175], off offset:128
	s_nop 1
	s_cbranch_vccz .Lt8zs_0
	ds_read_b128 v[168:171], v39
	ds_read_b128 v[172:175], v39 offset:1152
	s_waitcnt lgkmcnt(0)
	global_store_dwordx4 v[2:3], v[168:171], off
	global_store_dwordx4 v[198:199], v[172:175], off
	s_nop 1

.Lt8z_1_0:
	s_waitcnt lgkmcnt(1)
	global_store_dwordx4 v[194:195], v[168:171], off offset:256
	s_waitcnt lgkmcnt(0)
	global_store_dwordx4 v[196:197], v[172:175], off offset:256
	s_nop 1
	v_lshlrev_b32_e32 v168, 16, v26
	v_and_b32_e32 v169, 0xffff0000, v26
	v_lshlrev_b32_e32 v170, 16, v27
	v_and_b32_e32 v171, 0xffff0000, v27
	v_lshlrev_b32_e32 v172, 16, v28
	v_and_b32_e32 v173, 0xffff0000, v28
	v_lshlrev_b32_e32 v174, 16, v29
	v_and_b32_e32 v175, 0xffff0000, v29
	v_pk_mul_f32 v[168:169], v[4:5], v[168:169] op_sel_hi:[0,1]
	v_pk_mul_f32 v[170:171], v[4:5], v[170:171] op_sel_hi:[0,1]
	v_pk_fma_f32 v[116:117], v[184:185], v[116:117], v[168:169] op_sel_hi:[0,1,1]
	v_pk_fma_f32 v[118:119], v[184:185], v[118:119], v[170:171] op_sel_hi:[0,1,1]
	v_pk_mul_f32 v[116:117], v[116:117], v[172:173]
	v_pk_mul_f32 v[118:119], v[118:119], v[174:175]
	v_cvt_pk_bf16_f32 v240, v116, v117
	v_cvt_pk_bf16_f32 v241, v118, v119
	ds_write_b64 v0, v[240:241]
	v_lshlrev_b32_e32 v168, 16, v30
	v_and_b32_e32 v169, 0xffff0000, v30
	v_lshlrev_b32_e32 v170, 16, v31
	v_and_b32_e32 v171, 0xffff0000, v31
	v_lshlrev_b32_e32 v172, 16, v32
	v_and_b32_e32 v173, 0xffff0000, v32
	v_lshlrev_b32_e32 v174, 16, v33
	v_and_b32_e32 v175, 0xffff0000, v33
	v_pk_mul_f32 v[168:169], v[4:5], v[168:169] op_sel_hi:[0,1]
	v_pk_mul_f32 v[170:171], v[4:5], v[170:171] op_sel_hi:[0,1]
	v_pk_fma_f32 v[112:113], v[184:185], v[112:113], v[168:169] op_sel_hi:[0,1,1]
	v_pk_fma_f32 v[114:115], v[184:185], v[114:115], v[170:171] op_sel_hi:[0,1,1]
	v_pk_mul_f32 v[112:113], v[112:113], v[172:173]
	v_pk_mul_f32 v[114:115], v[114:115], v[174:175]
	v_cvt_pk_bf16_f32 v240, v112, v113
	v_cvt_pk_bf16_f32 v241, v114, v115
	ds_write_b64 v0, v[240:241] offset:32
	v_lshlrev_b32_e32 v168, 16, v34
	v_and_b32_e32 v169, 0xffff0000, v34
	v_lshlrev_b32_e32 v170, 16, v35
	v_and_b32_e32 v171, 0xffff0000, v35
	v_lshlrev_b32_e32 v172, 16, v36
	v_and_b32_e32 v173, 0xffff0000, v36
	v_lshlrev_b32_e32 v174, 16, v37
	v_and_b32_e32 v175, 0xffff0000, v37
	v_pk_mul_f32 v[168:169], v[4:5], v[168:169] op_sel_hi:[0,1]
	v_pk_mul_f32 v[170:171], v[4:5], v[170:171] op_sel_hi:[0,1]
	v_pk_fma_f32 v[108:109], v[184:185], v[108:109], v[168:169] op_sel_hi:[0,1,1]
	v_pk_fma_f32 v[110:111], v[184:185], v[110:111], v[170:171] op_sel_hi:[0,1,1]
	v_pk_mul_f32 v[108:109], v[108:109], v[172:173]
	v_pk_mul_f32 v[110:111], v[110:111], v[174:175]
	v_cvt_pk_bf16_f32 v240, v108, v109
	v_cvt_pk_bf16_f32 v241, v110, v111
	ds_write_b64 v0, v[240:241] offset:64
	v_lshlrev_b32_e32 v168, 16, v236
	v_and_b32_e32 v169, 0xffff0000, v236
	v_lshlrev_b32_e32 v170, 16, v237
	v_and_b32_e32 v171, 0xffff0000, v237
	v_lshlrev_b32_e32 v172, 16, v238
	v_and_b32_e32 v173, 0xffff0000, v238
	v_lshlrev_b32_e32 v174, 16, v239
	v_and_b32_e32 v175, 0xffff0000, v239
	v_pk_mul_f32 v[168:169], v[4:5], v[168:169] op_sel_hi:[0,1]
	v_pk_mul_f32 v[170:171], v[4:5], v[170:171] op_sel_hi:[0,1]
	v_pk_fma_f32 v[104:105], v[184:185], v[104:105], v[168:169] op_sel_hi:[0,1,1]
	v_pk_fma_f32 v[106:107], v[184:185], v[106:107], v[170:171] op_sel_hi:[0,1,1]
	v_pk_mul_f32 v[104:105], v[104:105], v[172:173]
	v_pk_mul_f32 v[106:107], v[106:107], v[174:175]
	v_cvt_pk_bf16_f32 v240, v104, v105
	v_cvt_pk_bf16_f32 v241, v106, v107
	ds_write_b64 v0, v[240:241] offset:96
	ds_read_b128 v[168:171], v1
	ds_read_b128 v[172:175], v1 offset:1152
	s_cbranch_vccz .Lt8z_1_1
	v_med3_f32 v248, v116, s77, v252
	v_med3_f32 v249, v117, s77, v252
	v_med3_f32 v250, v118, s77, v252
	v_med3_f32 v251, v119, s77, v252
	v_mov_b32_e32 v246, v245
	v_cvt_pk_fp8_f32 v246, v248, v249
	v_cvt_pk_fp8_f32 v246, v250, v251 op_sel:[0,0,1]
	ds_write_b32 v38, v246 offset:64
	v_med3_f32 v248, v112, s77, v252
	v_med3_f32 v249, v113, s77, v252
	v_med3_f32 v250, v114, s77, v252
	v_med3_f32 v251, v115, s77, v252
	v_mov_b32_e32 v246, v245
	v_cvt_pk_fp8_f32 v246, v248, v249
	v_cvt_pk_fp8_f32 v246, v250, v251 op_sel:[0,0,1]
	ds_write_b32 v38, v246 offset:80
	v_med3_f32 v248, v108, s77, v252
	v_med3_f32 v249, v109, s77, v252
	v_med3_f32 v250, v110, s77, v252
	v_med3_f32 v251, v111, s77, v252
	v_mov_b32_e32 v246, v245
	v_cvt_pk_fp8_f32 v246, v248, v249
	v_cvt_pk_fp8_f32 v246, v250, v251 op_sel:[0,0,1]
	ds_write_b32 v38, v246 offset:96
	v_med3_f32 v248, v104, s77, v252
	v_med3_f32 v249, v105, s77, v252
	v_med3_f32 v250, v106, s77, v252
	v_med3_f32 v251, v107, s77, v252
	v_mov_b32_e32 v246, v245
	v_cvt_pk_fp8_f32 v246, v248, v249
	v_cvt_pk_fp8_f32 v246, v250, v251 op_sel:[0,0,1]
	ds_write_b32 v38, v246 offset:112
.Lt8z_1_1:
	s_waitcnt lgkmcnt(1)
	global_store_dwordx4 v[194:195], v[168:171], off offset:384
	s_waitcnt lgkmcnt(0)
	global_store_dwordx4 v[196:197], v[172:175], off offset:384
	s_nop 1
	s_cbranch_vccz .Lt8zs_1
	ds_read_b128 v[168:171], v39
	ds_read_b128 v[172:175], v39 offset:1152
	s_waitcnt lgkmcnt(0)
	global_store_dwordx4 v[2:3], v[168:171], off offset:128
	global_store_dwordx4 v[198:199], v[172:175], off offset:128
	s_nop 1

.Lt8z_2_0:
	s_waitcnt lgkmcnt(1)
	global_store_dwordx4 v[194:195], v[168:171], off offset:512
	s_waitcnt lgkmcnt(0)
	global_store_dwordx4 v[196:197], v[172:175], off offset:512
	s_nop 1
	v_lshlrev_b32_e32 v168, 16, v26
	v_and_b32_e32 v169, 0xffff0000, v26
	v_lshlrev_b32_e32 v170, 16, v27
	v_and_b32_e32 v171, 0xffff0000, v27
	v_lshlrev_b32_e32 v172, 16, v28
	v_and_b32_e32 v173, 0xffff0000, v28
	v_lshlrev_b32_e32 v174, 16, v29
	v_and_b32_e32 v175, 0xffff0000, v29
	v_pk_mul_f32 v[168:169], v[4:5], v[168:169] op_sel_hi:[0,1]
	v_pk_mul_f32 v[170:171], v[4:5], v[170:171] op_sel_hi:[0,1]
	v_pk_fma_f32 v[84:85], v[184:185], v[84:85], v[168:169] op_sel_hi:[0,1,1]
	v_pk_fma_f32 v[86:87], v[184:185], v[86:87], v[170:171] op_sel_hi:[0,1,1]
	v_pk_mul_f32 v[84:85], v[84:85], v[172:173]
	v_pk_mul_f32 v[86:87], v[86:87], v[174:175]
	v_cvt_pk_bf16_f32 v240, v84, v85
	v_cvt_pk_bf16_f32 v241, v86, v87
	ds_write_b64 v0, v[240:241]
	v_lshlrev_b32_e32 v168, 16, v30
	v_and_b32_e32 v169, 0xffff0000, v30
	v_lshlrev_b32_e32 v170, 16, v31
	v_and_b32_e32 v171, 0xffff0000, v31
	v_lshlrev_b32_e32 v172, 16, v32
	v_and_b32_e32 v173, 0xffff0000, v32
	v_lshlrev_b32_e32 v174, 16, v33
	v_and_b32_e32 v175, 0xffff0000, v33
	v_pk_mul_f32 v[168:169], v[4:5], v[168:169] op_sel_hi:[0,1]
	v_pk_mul_f32 v[170:171], v[4:5], v[170:171] op_sel_hi:[0,1]
	v_pk_fma_f32 v[80:81], v[184:185], v[80:81], v[168:169] op_sel_hi:[0,1,1]
	v_pk_fma_f32 v[82:83], v[184:185], v[82:83], v[170:171] op_sel_hi:[0,1,1]
	v_pk_mul_f32 v[80:81], v[80:81], v[172:173]
	v_pk_mul_f32 v[82:83], v[82:83], v[174:175]
	v_cvt_pk_bf16_f32 v240, v80, v81
	v_cvt_pk_bf16_f32 v241, v82, v83
	ds_write_b64 v0, v[240:241] offset:32
	v_lshlrev_b32_e32 v168, 16, v34
	v_and_b32_e32 v169, 0xffff0000, v34
	v_lshlrev_b32_e32 v170, 16, v35
	v_and_b32_e32 v171, 0xffff0000, v35
	v_lshlrev_b32_e32 v172, 16, v36
	v_and_b32_e32 v173, 0xffff0000, v36
	v_lshlrev_b32_e32 v174, 16, v37
	v_and_b32_e32 v175, 0xffff0000, v37
	v_pk_mul_f32 v[168:169], v[4:5], v[168:169] op_sel_hi:[0,1]
	v_pk_mul_f32 v[170:171], v[4:5], v[170:171] op_sel_hi:[0,1]
	v_pk_fma_f32 v[76:77], v[184:185], v[76:77], v[168:169] op_sel_hi:[0,1,1]
	v_pk_fma_f32 v[78:79], v[184:185], v[78:79], v[170:171] op_sel_hi:[0,1,1]
	v_pk_mul_f32 v[76:77], v[76:77], v[172:173]
	v_pk_mul_f32 v[78:79], v[78:79], v[174:175]
	v_cvt_pk_bf16_f32 v240, v76, v77
	v_cvt_pk_bf16_f32 v241, v78, v79
	ds_write_b64 v0, v[240:241] offset:64
	v_lshlrev_b32_e32 v168, 16, v236
	v_and_b32_e32 v169, 0xffff0000, v236
	v_lshlrev_b32_e32 v170, 16, v237
	v_and_b32_e32 v171, 0xffff0000, v237
	v_lshlrev_b32_e32 v172, 16, v238
	v_and_b32_e32 v173, 0xffff0000, v238
	v_lshlrev_b32_e32 v174, 16, v239
	v_and_b32_e32 v175, 0xffff0000, v239
	v_pk_mul_f32 v[168:169], v[4:5], v[168:169] op_sel_hi:[0,1]
	v_pk_mul_f32 v[170:171], v[4:5], v[170:171] op_sel_hi:[0,1]
	v_pk_fma_f32 v[72:73], v[184:185], v[72:73], v[168:169] op_sel_hi:[0,1,1]
	v_pk_fma_f32 v[74:75], v[184:185], v[74:75], v[170:171] op_sel_hi:[0,1,1]
	v_pk_mul_f32 v[72:73], v[72:73], v[172:173]
	v_pk_mul_f32 v[74:75], v[74:75], v[174:175]
	v_cvt_pk_bf16_f32 v240, v72, v73
	v_cvt_pk_bf16_f32 v241, v74, v75
	ds_write_b64 v0, v[240:241] offset:96
	ds_read_b128 v[168:171], v1
	ds_read_b128 v[172:175], v1 offset:1152
	s_cbranch_vccz .Lt8z_2_1
	v_med3_f32 v248, v84, s77, v252
	v_med3_f32 v249, v85, s77, v252
	v_med3_f32 v250, v86, s77, v252
	v_med3_f32 v251, v87, s77, v252
	v_mov_b32_e32 v246, v245
	v_cvt_pk_fp8_f32 v246, v248, v249
	v_cvt_pk_fp8_f32 v246, v250, v251 op_sel:[0,0,1]
	ds_write_b32 v38, v246 offset:64
	v_med3_f32 v248, v80, s77, v252
	v_med3_f32 v249, v81, s77, v252
	v_med3_f32 v250, v82, s77, v252
	v_med3_f32 v251, v83, s77, v252
	v_mov_b32_e32 v246, v245
	v_cvt_pk_fp8_f32 v246, v248, v249
	v_cvt_pk_fp8_f32 v246, v250, v251 op_sel:[0,0,1]
	ds_write_b32 v38, v246 offset:80
	v_med3_f32 v248, v76, s77, v252
	v_med3_f32 v249, v77, s77, v252
	v_med3_f32 v250, v78, s77, v252
	v_med3_f32 v251, v79, s77, v252
	v_mov_b32_e32 v246, v245
	v_cvt_pk_fp8_f32 v246, v248, v249
	v_cvt_pk_fp8_f32 v246, v250, v251 op_sel:[0,0,1]
	ds_write_b32 v38, v246 offset:96
	v_med3_f32 v248, v72, s77, v252
	v_med3_f32 v249, v73, s77, v252
	v_med3_f32 v250, v74, s77, v252
	v_med3_f32 v251, v75, s77, v252
	v_mov_b32_e32 v246, v245
	v_cvt_pk_fp8_f32 v246, v248, v249
	v_cvt_pk_fp8_f32 v246, v250, v251 op_sel:[0,0,1]
	ds_write_b32 v38, v246 offset:112
.Lt8z_2_1:
	s_waitcnt lgkmcnt(1)
	global_store_dwordx4 v[194:195], v[168:171], off offset:640
	s_waitcnt lgkmcnt(0)
	global_store_dwordx4 v[196:197], v[172:175], off offset:640
	s_nop 1
	s_cbranch_vccz .Lt8zs_2
	ds_read_b128 v[168:171], v39
	ds_read_b128 v[172:175], v39 offset:1152
	s_waitcnt lgkmcnt(0)
	global_store_dwordx4 v[2:3], v[168:171], off offset:256
	global_store_dwordx4 v[198:199], v[172:175], off offset:256
	s_nop 1

.Lt8z_3_0:
	s_waitcnt lgkmcnt(1)
	global_store_dwordx4 v[194:195], v[168:171], off offset:768
	s_waitcnt lgkmcnt(0)
	global_store_dwordx4 v[196:197], v[172:175], off offset:768
	s_nop 1
	v_lshlrev_b32_e32 v168, 16, v26
	v_and_b32_e32 v169, 0xffff0000, v26
	v_lshlrev_b32_e32 v170, 16, v27
	v_and_b32_e32 v171, 0xffff0000, v27
	v_lshlrev_b32_e32 v172, 16, v28
	v_and_b32_e32 v173, 0xffff0000, v28
	v_lshlrev_b32_e32 v174, 16, v29
	v_and_b32_e32 v175, 0xffff0000, v29
	v_pk_mul_f32 v[168:169], v[4:5], v[168:169] op_sel_hi:[0,1]
	v_pk_mul_f32 v[170:171], v[4:5], v[170:171] op_sel_hi:[0,1]
	v_pk_fma_f32 v[52:53], v[184:185], v[52:53], v[168:169] op_sel_hi:[0,1,1]
	v_pk_fma_f32 v[54:55], v[184:185], v[54:55], v[170:171] op_sel_hi:[0,1,1]
	v_pk_mul_f32 v[52:53], v[52:53], v[172:173]
	v_pk_mul_f32 v[54:55], v[54:55], v[174:175]
	v_cvt_pk_bf16_f32 v240, v52, v53
	v_cvt_pk_bf16_f32 v241, v54, v55
	ds_write_b64 v0, v[240:241]
	v_lshlrev_b32_e32 v168, 16, v30
	v_and_b32_e32 v169, 0xffff0000, v30
	v_lshlrev_b32_e32 v170, 16, v31
	v_and_b32_e32 v171, 0xffff0000, v31
	v_lshlrev_b32_e32 v172, 16, v32
	v_and_b32_e32 v173, 0xffff0000, v32
	v_lshlrev_b32_e32 v174, 16, v33
	v_and_b32_e32 v175, 0xffff0000, v33
	v_pk_mul_f32 v[168:169], v[4:5], v[168:169] op_sel_hi:[0,1]
	v_pk_mul_f32 v[170:171], v[4:5], v[170:171] op_sel_hi:[0,1]
	v_pk_fma_f32 v[48:49], v[184:185], v[48:49], v[168:169] op_sel_hi:[0,1,1]
	v_pk_fma_f32 v[50:51], v[184:185], v[50:51], v[170:171] op_sel_hi:[0,1,1]
	v_pk_mul_f32 v[48:49], v[48:49], v[172:173]
	v_pk_mul_f32 v[50:51], v[50:51], v[174:175]
	v_cvt_pk_bf16_f32 v240, v48, v49
	v_cvt_pk_bf16_f32 v241, v50, v51
	ds_write_b64 v0, v[240:241] offset:32
	v_lshlrev_b32_e32 v168, 16, v34
	v_and_b32_e32 v169, 0xffff0000, v34
	v_lshlrev_b32_e32 v170, 16, v35
	v_and_b32_e32 v171, 0xffff0000, v35
	v_lshlrev_b32_e32 v172, 16, v36
	v_and_b32_e32 v173, 0xffff0000, v36
	v_lshlrev_b32_e32 v174, 16, v37
	v_and_b32_e32 v175, 0xffff0000, v37
	v_pk_mul_f32 v[168:169], v[4:5], v[168:169] op_sel_hi:[0,1]
	v_pk_mul_f32 v[170:171], v[4:5], v[170:171] op_sel_hi:[0,1]
	v_pk_fma_f32 v[44:45], v[184:185], v[44:45], v[168:169] op_sel_hi:[0,1,1]
	v_pk_fma_f32 v[46:47], v[184:185], v[46:47], v[170:171] op_sel_hi:[0,1,1]
	v_pk_mul_f32 v[44:45], v[44:45], v[172:173]
	v_pk_mul_f32 v[46:47], v[46:47], v[174:175]
	v_cvt_pk_bf16_f32 v240, v44, v45
	v_cvt_pk_bf16_f32 v241, v46, v47
	ds_write_b64 v0, v[240:241] offset:64
	v_lshlrev_b32_e32 v168, 16, v236
	v_and_b32_e32 v169, 0xffff0000, v236
	v_lshlrev_b32_e32 v170, 16, v237
	v_and_b32_e32 v171, 0xffff0000, v237
	v_lshlrev_b32_e32 v172, 16, v238
	v_and_b32_e32 v173, 0xffff0000, v238
	v_lshlrev_b32_e32 v174, 16, v239
	v_and_b32_e32 v175, 0xffff0000, v239
	v_pk_mul_f32 v[168:169], v[4:5], v[168:169] op_sel_hi:[0,1]
	v_pk_mul_f32 v[170:171], v[4:5], v[170:171] op_sel_hi:[0,1]
	v_pk_fma_f32 v[40:41], v[184:185], v[40:41], v[168:169] op_sel_hi:[0,1,1]
	v_pk_fma_f32 v[42:43], v[184:185], v[42:43], v[170:171] op_sel_hi:[0,1,1]
	v_pk_mul_f32 v[40:41], v[40:41], v[172:173]
	v_pk_mul_f32 v[42:43], v[42:43], v[174:175]
	v_cvt_pk_bf16_f32 v240, v40, v41
	v_cvt_pk_bf16_f32 v241, v42, v43
	ds_write_b64 v0, v[240:241] offset:96
	ds_read_b128 v[168:171], v1
	ds_read_b128 v[172:175], v1 offset:1152
	s_cbranch_vccz .Lt8z_3_1
	v_med3_f32 v248, v52, s77, v252
	v_med3_f32 v249, v53, s77, v252
	v_med3_f32 v250, v54, s77, v252
	v_med3_f32 v251, v55, s77, v252
	v_mov_b32_e32 v246, v245
	v_cvt_pk_fp8_f32 v246, v248, v249
	v_cvt_pk_fp8_f32 v246, v250, v251 op_sel:[0,0,1]
	ds_write_b32 v38, v246 offset:64
	v_med3_f32 v248, v48, s77, v252
	v_med3_f32 v249, v49, s77, v252
	v_med3_f32 v250, v50, s77, v252
	v_med3_f32 v251, v51, s77, v252
	v_mov_b32_e32 v246, v245
	v_cvt_pk_fp8_f32 v246, v248, v249
	v_cvt_pk_fp8_f32 v246, v250, v251 op_sel:[0,0,1]
	ds_write_b32 v38, v246 offset:80
	v_med3_f32 v248, v44, s77, v252
	v_med3_f32 v249, v45, s77, v252
	v_med3_f32 v250, v46, s77, v252
	v_med3_f32 v251, v47, s77, v252
	v_mov_b32_e32 v246, v245
	v_cvt_pk_fp8_f32 v246, v248, v249
	v_cvt_pk_fp8_f32 v246, v250, v251 op_sel:[0,0,1]
	ds_write_b32 v38, v246 offset:96
	v_med3_f32 v248, v40, s77, v252
	v_med3_f32 v249, v41, s77, v252
	v_med3_f32 v250, v42, s77, v252
	v_med3_f32 v251, v43, s77, v252
	v_mov_b32_e32 v246, v245
	v_cvt_pk_fp8_f32 v246, v248, v249
	v_cvt_pk_fp8_f32 v246, v250, v251 op_sel:[0,0,1]
	ds_write_b32 v38, v246 offset:112
.Lt8z_3_1:
	s_waitcnt lgkmcnt(1)
	global_store_dwordx4 v[194:195], v[168:171], off offset:896
	s_waitcnt lgkmcnt(0)
	global_store_dwordx4 v[196:197], v[172:175], off offset:896
	s_nop 1
	s_cbranch_vccz .Lt8zs_3
	ds_read_b128 v[168:171], v39
	ds_read_b128 v[172:175], v39 offset:1152
	s_waitcnt lgkmcnt(0)
	global_store_dwordx4 v[2:3], v[168:171], off offset:384
	global_store_dwordx4 v[198:199], v[172:175], off offset:384
	s_nop 1

.LBB0_624:
	s_add_i32 s62, s62, s55
	s_min_u32 s4, s34, 60
	v_med3_i32 v191, s62, 4, 60
	v_subrev_u32_e32 v84, s4, v191
	v_lshlrev_b32_e32 v153, 13, v84
	v_add_u16_e32 v86, s29, v154
	v_add_u32_e32 v85, s29, v154
	v_add_u32_e32 v84, 0, v153
	v_lshrrev_b16_e32 v88, 1, v86
	v_bitop3_b32 v86, v88, v155, 7 bitop3:0x6c
	v_lshl_add_u32 v89, v85, 7, v84
	v_lshl_add_u32 v196, v86, 4, v89
	v_bitop3_b32 v88, v88, v183, 7 bitop3:0x6c
	v_lshl_add_u32 v197, v88, 4, v89
	s_movk_i32 s4, 0x7c
	ds_read_b128 v[212:215], v196
	ds_read_b128 v[216:219], v197
	ds_read_b128 v[220:223], v196 offset:2048
	ds_read_b128 v[224:227], v197 offset:2048
	ds_read_b128 v[228:231], v196 offset:8192
	ds_read_b128 v[232:235], v197 offset:8192
	ds_read_b128 v[236:239], v196 offset:10240
	ds_read_b128 v[240:243], v197 offset:10240
	s_waitcnt lgkmcnt(6)
	v_mfma_f32_16x16x32_bf16 v[144:147], v[212:215], v[100:103], 0
	v_mfma_f32_16x16x32_bf16 v[144:147], v[216:219], v[80:83], v[144:147]
	ds_read_b128 v[212:215], v196 offset:16384
	ds_read_b128 v[216:219], v197 offset:16384
	s_waitcnt lgkmcnt(6)
	v_mfma_f32_16x16x32_bf16 v[140:143], v[220:223], v[100:103], 0
	v_mfma_f32_16x16x32_bf16 v[140:143], v[224:227], v[80:83], v[140:143]
	ds_read_b128 v[220:223], v196 offset:18432
	ds_read_b128 v[224:227], v197 offset:18432
	s_waitcnt lgkmcnt(6)
	v_mfma_f32_16x16x32_bf16 v[136:139], v[228:231], v[100:103], 0
	v_mfma_f32_16x16x32_bf16 v[136:139], v[232:235], v[80:83], v[136:139]
	ds_read_b128 v[228:231], v196 offset:24576
	ds_read_b128 v[232:235], v197 offset:24576
	s_waitcnt lgkmcnt(6)
	v_mfma_f32_16x16x32_bf16 v[132:135], v[236:239], v[100:103], 0
	v_mfma_f32_16x16x32_bf16 v[132:135], v[240:243], v[80:83], v[132:135]
	ds_read_b128 v[236:239], v196 offset:26624
	ds_read_b128 v[240:243], v197 offset:26624
	s_waitcnt lgkmcnt(6)
	v_mfma_f32_16x16x32_bf16 v[128:131], v[212:215], v[100:103], 0
	v_mfma_f32_16x16x32_bf16 v[128:131], v[216:219], v[80:83], v[128:131]
	ds_read_b128 v[212:215], v196 offset:32768
	ds_read_b128 v[216:219], v197 offset:32768
	s_waitcnt lgkmcnt(6)
	v_mfma_f32_16x16x32_bf16 v[124:127], v[220:223], v[100:103], 0
	v_mfma_f32_16x16x32_bf16 v[124:127], v[224:227], v[80:83], v[124:127]
	ds_read_b128 v[220:223], v196 offset:34816
	ds_read_b128 v[224:227], v197 offset:34816
	s_waitcnt lgkmcnt(6)
	v_mfma_f32_16x16x32_bf16 v[120:123], v[228:231], v[100:103], 0
	v_mfma_f32_16x16x32_bf16 v[120:123], v[232:235], v[80:83], v[120:123]
	ds_read_b128 v[228:231], v196 offset:40960
	ds_read_b128 v[232:235], v197 offset:40960
	s_waitcnt lgkmcnt(6)
	v_mfma_f32_16x16x32_bf16 v[116:119], v[236:239], v[100:103], 0
	v_mfma_f32_16x16x32_bf16 v[116:119], v[240:243], v[80:83], v[116:119]
	ds_read_b128 v[236:239], v196 offset:43008
	ds_read_b128 v[240:243], v197 offset:43008
	s_waitcnt lgkmcnt(6)
	v_mfma_f32_16x16x32_bf16 v[112:115], v[212:215], v[100:103], 0
	v_mfma_f32_16x16x32_bf16 v[112:115], v[216:219], v[80:83], v[112:115]
	ds_read_b128 v[212:215], v196 offset:49152
	ds_read_b128 v[216:219], v197 offset:49152
	s_waitcnt lgkmcnt(6)
	v_mfma_f32_16x16x32_bf16 v[108:111], v[220:223], v[100:103], 0
	v_mfma_f32_16x16x32_bf16 v[108:111], v[224:227], v[80:83], v[108:111]
	ds_read_b128 v[220:223], v196 offset:51200
	ds_read_b128 v[224:227], v197 offset:51200
	s_waitcnt lgkmcnt(6)
	v_mfma_f32_16x16x32_bf16 v[104:107], v[228:231], v[100:103], 0
	v_mfma_f32_16x16x32_bf16 v[104:107], v[232:235], v[80:83], v[104:107]
	ds_read_b128 v[228:231], v196 offset:57344
	ds_read_b128 v[232:235], v197 offset:57344
	s_waitcnt lgkmcnt(6)
	v_mfma_f32_16x16x32_bf16 v[96:99], v[236:239], v[100:103], 0
	v_mfma_f32_16x16x32_bf16 v[96:99], v[240:243], v[80:83], v[96:99]
	ds_read_b128 v[236:239], v196 offset:59392
	ds_read_b128 v[240:243], v197 offset:59392
	s_waitcnt lgkmcnt(6)
	v_mfma_f32_16x16x32_bf16 v[92:95], v[212:215], v[100:103], 0
	v_mfma_f32_16x16x32_bf16 v[92:95], v[216:219], v[80:83], v[92:95]
	s_waitcnt lgkmcnt(4)
	v_mfma_f32_16x16x32_bf16 v[88:91], v[220:223], v[100:103], 0
	v_mfma_f32_16x16x32_bf16 v[88:91], v[224:227], v[80:83], v[88:91]
	s_waitcnt lgkmcnt(2)
	v_mfma_f32_16x16x32_bf16 v[84:87], v[228:231], v[100:103], 0
	v_mfma_f32_16x16x32_bf16 v[84:87], v[232:235], v[80:83], v[84:87]
	s_waitcnt lgkmcnt(0)
	v_mfma_f32_16x16x32_bf16 v[192:195], v[236:239], v[100:103], 0
	v_mfma_f32_16x16x32_bf16 v[80:83], v[240:243], v[80:83], v[192:195]
	v_add_u32_e32 v246, s29, v148
	v_subrev_u32_e32 v247, s62, v191
	v_mul_lo_u32 v247, v247, s4
	v_sub_u32_e32 v248, v246, v150
	v_lshl_add_u32 v247, v248, 2, v247
	v_add_u32_e32 v247, 0x23e10, v247
	v_cmp_ge_u32_e32 vcc, v246, v188
	v_cmp_lt_u32_e64 s[4:5], v246, v189
	s_and_b64 s[30:31], vcc, s[4:5]
	v_or_b32_e32 v248, 1, v246
	v_cmp_ge_u32_e32 vcc, v248, v188
	v_cmp_lt_u32_e64 s[4:5], v248, v189
	s_and_b64 s[34:35], vcc, s[4:5]
	v_or_b32_e32 v248, 2, v246
	v_cmp_ge_u32_e32 vcc, v248, v188
	v_cmp_lt_u32_e64 s[4:5], v248, v189
	s_and_b64 s[36:37], vcc, s[4:5]
	v_or_b32_e32 v248, 3, v246
	v_cmp_ge_u32_e32 vcc, v248, v188
	v_cmp_lt_u32_e64 s[4:5], v248, v189
	s_and_b64 s[38:39], vcc, s[4:5]
	v_add_u32_e32 v248, 16, v246
	v_cmp_ge_u32_e32 vcc, v248, v188
	v_cmp_lt_u32_e64 s[4:5], v248, v189
	s_and_b64 s[40:41], vcc, s[4:5]
	v_add_u32_e32 v248, 17, v246
	v_cmp_ge_u32_e32 vcc, v248, v188
	v_cmp_lt_u32_e64 s[4:5], v248, v189
	s_and_b64 s[42:43], vcc, s[4:5]
	v_add_u32_e32 v248, 18, v246
	v_cmp_ge_u32_e32 vcc, v248, v188
	v_cmp_lt_u32_e64 s[4:5], v248, v189
	s_and_b64 s[44:45], vcc, s[4:5]
	v_add_u32_e32 v248, 19, v246
	v_cmp_ge_u32_e32 vcc, v248, v188
	v_cmp_lt_u32_e64 s[4:5], v248, v189
	s_and_b64 s[4:5], vcc, s[4:5]
	v_mov_b32_e32 v248, 64
	v_mov_b32_e32 v249, 0xff800000
	v_cndmask_b32_e64 v250, v248, 0, s[30:31]
	v_cndmask_b32_e64 v251, v248, 0, s[34:35]
	v_cndmask_b32_e64 v252, v248, 0, s[36:37]
	v_cndmask_b32_e64 v246, v248, 0, s[38:39]
	v_add3_u32 v250, v250, v247, 0
	v_add3_u32 v251, v251, v247, 4
	v_add3_u32 v252, v252, v247, 8
	v_add3_u32 v246, v246, v247, 12
	ds_read_b32 v212, v250 offset:928
	ds_read_b32 v213, v251 offset:928
	ds_read_b32 v214, v252 offset:928
	ds_read_b32 v215, v246 offset:928
	ds_read_b32 v216, v250 offset:1052
	ds_read_b32 v217, v251 offset:1052
	ds_read_b32 v218, v252 offset:1052
	ds_read_b32 v219, v246 offset:1052
	ds_read_b32 v220, v250 offset:1176
	ds_read_b32 v221, v251 offset:1176
	ds_read_b32 v222, v252 offset:1176
	ds_read_b32 v223, v246 offset:1176
	ds_read_b32 v224, v250 offset:1300
	ds_read_b32 v225, v251 offset:1300
	ds_read_b32 v226, v252 offset:1300
	ds_read_b32 v227, v246 offset:1300
	ds_read_b32 v228, v250 offset:1424
	ds_read_b32 v229, v251 offset:1424
	ds_read_b32 v230, v252 offset:1424
	ds_read_b32 v231, v246 offset:1424
	ds_read_b32 v232, v250 offset:1548
	ds_read_b32 v233, v251 offset:1548
	ds_read_b32 v234, v252 offset:1548
	ds_read_b32 v235, v246 offset:1548
	ds_read_b32 v236, v250 offset:1672
	ds_read_b32 v237, v251 offset:1672
	ds_read_b32 v238, v252 offset:1672
	ds_read_b32 v239, v246 offset:1672
	ds_read_b32 v240, v250 offset:1796
	ds_read_b32 v241, v251 offset:1796
	ds_read_b32 v242, v252 offset:1796
	ds_read_b32 v243, v246 offset:1796
	s_waitcnt lgkmcnt(15)
	v_add_f32_e32 v101, v144, v212
	v_cndmask_b32_e64 v101, v249, v101, s[30:31]
	v_add_f32_e32 v100, v145, v213
	v_cndmask_b32_e64 v100, v249, v100, s[34:35]
	v_add_f32_e32 v103, v146, v214
	v_cndmask_b32_e64 v103, v249, v103, s[36:37]
	v_add_f32_e32 v102, v147, v215
	v_cndmask_b32_e64 v102, v249, v102, s[38:39]
	v_add_f32_e32 v145, v140, v212
	v_cndmask_b32_e64 v145, v249, v145, s[40:41]
	v_add_f32_e32 v144, v141, v213
	v_cndmask_b32_e64 v144, v249, v144, s[42:43]
	v_add_f32_e32 v146, v142, v214
	v_cndmask_b32_e64 v146, v249, v146, s[44:45]
	v_add_f32_e32 v140, v143, v215
	v_cndmask_b32_e64 v140, v249, v140, s[4:5]
	s_waitcnt lgkmcnt(15)
	v_add_f32_e32 v142, v136, v216
	v_cndmask_b32_e64 v142, v249, v142, s[30:31]
	v_add_f32_e32 v141, v137, v217
	v_cndmask_b32_e64 v141, v249, v141, s[34:35]
	v_add_f32_e32 v137, v138, v218
	v_cndmask_b32_e64 v137, v249, v137, s[36:37]
	v_add_f32_e32 v136, v139, v219
	v_cndmask_b32_e64 v136, v249, v136, s[38:39]
	v_add_f32_e32 v139, v132, v216
	v_cndmask_b32_e64 v139, v249, v139, s[40:41]
	v_add_f32_e32 v138, v133, v217
	v_cndmask_b32_e64 v138, v249, v138, s[42:43]
	v_add_f32_e32 v133, v134, v218
	v_cndmask_b32_e64 v133, v249, v133, s[44:45]
	v_add_f32_e32 v132, v135, v219
	v_cndmask_b32_e64 v132, v249, v132, s[4:5]
	s_waitcnt lgkmcnt(15)
	v_add_f32_e32 v135, v128, v220
	v_cndmask_b32_e64 v135, v249, v135, s[30:31]
	v_add_f32_e32 v134, v129, v221
	v_cndmask_b32_e64 v134, v249, v134, s[34:35]
	v_add_f32_e32 v129, v130, v222
	v_cndmask_b32_e64 v129, v249, v129, s[36:37]
	v_add_f32_e32 v128, v131, v223
	v_cndmask_b32_e64 v128, v249, v128, s[38:39]
	v_add_f32_e32 v131, v124, v220
	v_cndmask_b32_e64 v131, v249, v131, s[40:41]
	v_add_f32_e32 v130, v125, v221
	v_cndmask_b32_e64 v130, v249, v130, s[42:43]
	v_add_f32_e32 v125, v126, v222
	v_cndmask_b32_e64 v125, v249, v125, s[44:45]
	v_add_f32_e32 v124, v127, v223
	v_cndmask_b32_e64 v124, v249, v124, s[4:5]
	s_waitcnt lgkmcnt(15)
	v_add_f32_e32 v127, v120, v224
	v_cndmask_b32_e64 v127, v249, v127, s[30:31]
	v_add_f32_e32 v126, v121, v225
	v_cndmask_b32_e64 v126, v249, v126, s[34:35]
	v_add_f32_e32 v121, v122, v226
	v_cndmask_b32_e64 v121, v249, v121, s[36:37]
	v_add_f32_e32 v120, v123, v227
	v_cndmask_b32_e64 v120, v249, v120, s[38:39]
	v_add_f32_e32 v123, v116, v224
	v_cndmask_b32_e64 v123, v249, v123, s[40:41]
	v_add_f32_e32 v122, v117, v225
	v_cndmask_b32_e64 v122, v249, v122, s[42:43]
	v_add_f32_e32 v117, v118, v226
	v_cndmask_b32_e64 v117, v249, v117, s[44:45]
	v_add_f32_e32 v116, v119, v227
	v_cndmask_b32_e64 v116, v249, v116, s[4:5]
	s_waitcnt lgkmcnt(12)
	v_add_f32_e32 v119, v112, v228
	v_cndmask_b32_e64 v119, v249, v119, s[30:31]
	v_add_f32_e32 v118, v113, v229
	v_cndmask_b32_e64 v118, v249, v118, s[34:35]
	v_add_f32_e32 v147, v114, v230
	v_cndmask_b32_e64 v147, v249, v147, s[36:37]
	v_add_f32_e32 v112, v115, v231
	v_cndmask_b32_e64 v112, v249, v112, s[38:39]
	v_add_f32_e32 v192, v108, v228
	v_cndmask_b32_e64 v192, v249, v192, s[40:41]
	v_add_f32_e32 v114, v109, v229
	v_cndmask_b32_e64 v114, v249, v114, s[42:43]
	v_add_f32_e32 v193, v110, v230
	v_cndmask_b32_e64 v193, v249, v193, s[44:45]
	v_add_f32_e32 v109, v111, v231
	v_cndmask_b32_e64 v109, v249, v109, s[4:5]
	s_waitcnt lgkmcnt(8)
	v_add_f32_e32 v194, v104, v232
	v_cndmask_b32_e64 v194, v249, v194, s[30:31]
	v_add_f32_e32 v111, v105, v233
	v_cndmask_b32_e64 v111, v249, v111, s[34:35]
	v_add_f32_e32 v105, v106, v234
	v_cndmask_b32_e64 v105, v249, v105, s[36:37]
	v_add_f32_e32 v104, v107, v235
	v_cndmask_b32_e64 v104, v249, v104, s[38:39]
	v_add_f32_e32 v196, v96, v232
	v_cndmask_b32_e64 v196, v249, v196, s[40:41]
	v_add_f32_e32 v195, v97, v233
	v_cndmask_b32_e64 v195, v249, v195, s[42:43]
	v_add_f32_e32 v97, v98, v234
	v_cndmask_b32_e64 v97, v249, v97, s[44:45]
	v_add_f32_e32 v96, v99, v235
	v_cndmask_b32_e64 v96, v249, v96, s[4:5]
	s_waitcnt lgkmcnt(4)
	v_add_f32_e32 v99, v92, v236
	v_cndmask_b32_e64 v99, v249, v99, s[30:31]
	v_add_f32_e32 v98, v93, v237
	v_cndmask_b32_e64 v98, v249, v98, s[34:35]
	v_add_f32_e32 v93, v94, v238
	v_cndmask_b32_e64 v93, v249, v93, s[36:37]
	v_add_f32_e32 v92, v95, v239
	v_cndmask_b32_e64 v92, v249, v92, s[38:39]
	v_add_f32_e32 v95, v88, v236
	v_cndmask_b32_e64 v95, v249, v95, s[40:41]
	v_add_f32_e32 v94, v89, v237
	v_cndmask_b32_e64 v94, v249, v94, s[42:43]
	v_add_f32_e32 v89, v90, v238
	v_cndmask_b32_e64 v89, v249, v89, s[44:45]
	v_add_f32_e32 v88, v91, v239
	v_cndmask_b32_e64 v88, v249, v88, s[4:5]
	s_waitcnt lgkmcnt(0)
	v_add_f32_e32 v91, v84, v240
	v_cndmask_b32_e64 v91, v249, v91, s[30:31]
	v_add_f32_e32 v90, v85, v241
	v_cndmask_b32_e64 v90, v249, v90, s[34:35]
	v_add_f32_e32 v198, v86, v242
	v_cndmask_b32_e64 v198, v249, v198, s[36:37]
	v_add_f32_e32 v197, v87, v243
	v_cndmask_b32_e64 v197, v249, v197, s[38:39]
	v_add_f32_e32 v202, v80, v240
	v_cndmask_b32_e64 v202, v249, v202, s[40:41]
	v_add_f32_e32 v199, v81, v241
	v_cndmask_b32_e64 v199, v249, v199, s[42:43]
	v_add_f32_e32 v81, v82, v242
	v_cndmask_b32_e64 v81, v249, v81, s[44:45]
	v_add_f32_e32 v80, v83, v243
	v_cndmask_b32_e64 v80, v249, v80, s[4:5]
	s_branch .LBB0_614
	s_nop 0
	s_nop 0
	s_nop 0
	s_nop 0
	s_nop 0
	s_nop 0
	s_nop 0
	s_nop 0
	s_nop 0
	s_nop 0
	s_nop 0
	s_nop 0
	s_nop 0
	s_nop 0
	s_nop 0
	s_nop 0
